# v24 + diff-attention LDS-DMA of tile j+2 issued one instruction per MFMA group inside the wave's P.V pass instead of a burst behind the tile barrier
# speedup vs baseline: 1.0037x; 1.0037x over previous
.LBB0_185:
	s_andn2_b64 vcc, exec, s[42:43]
	s_cbranch_vccz .LBB0_192
.LBB0_186:
	s_cmp_eq_u32 s71, 0
	s_cbranch_scc1 .LBB0_193
.LBB0_187:
	s_cmp_eq_u32 s71, 0
	s_cbranch_scc1 .LBB0_189
.LBB0_188:
	s_waitcnt lgkmcnt(0)
	v_add_u32_e32 v0, s44, v224
	ds_read_b64_tr_b16 v[160:161], v0 offset:0
	ds_read_b64_tr_b16 v[162:163], v0 offset:0x800
	ds_read_b64_tr_b16 v[164:165], v0 offset:0x200
	ds_read_b64_tr_b16 v[166:167], v0 offset:0xa00
	ds_read_b64_tr_b16 v[168:169], v0 offset:0x400
	ds_read_b64_tr_b16 v[170:171], v0 offset:0xc00
	ds_read_b64_tr_b16 v[172:173], v0 offset:0x600
	ds_read_b64_tr_b16 v[174:175], v0 offset:0xe00
	s_waitcnt lgkmcnt(4)
	s_nop 0
	v_mfma_f32_32x32x16_bf16 v[112:127], v[208:211], v[160:163], v[112:127]
	v_mfma_f32_32x32x16_bf16 v[96:111], v[208:211], v[164:167], v[96:111]
	v_mfma_f32_32x32x16_bf16 v[128:143], v[156:159], v[160:163], v[128:143]
	v_mfma_f32_32x32x16_bf16 v[80:95], v[156:159], v[164:167], v[80:95]
	s_cmp_gt_u32 s86, 61
	s_cbranch_scc1 .Ldmab1
	s_add_i32 s42, s7, s90
	v_lshl_add_u64 v[252:253], s[40:41], 0, v[218:219]
	s_mov_b32 m0, s42
	s_nop 0
	global_load_lds_dwordx4 v[252:253], off
.Ldmab1:
	ds_read_b64_tr_b16 v[160:161], v0 offset:0x1000
	ds_read_b64_tr_b16 v[162:163], v0 offset:0x1800
	ds_read_b64_tr_b16 v[164:165], v0 offset:0x1200
	ds_read_b64_tr_b16 v[166:167], v0 offset:0x1a00
	s_waitcnt lgkmcnt(4)
	v_mfma_f32_32x32x16_bf16 v[64:79], v[208:211], v[168:171], v[64:79]
	v_mfma_f32_32x32x16_bf16 v[48:63], v[208:211], v[172:175], v[48:63]
	v_mfma_f32_32x32x16_bf16 v[32:47], v[156:159], v[168:171], v[32:47]
	v_mfma_f32_32x32x16_bf16 v[16:31], v[156:159], v[172:175], v[16:31]
	s_cmp_gt_u32 s86, 61
	s_cbranch_scc1 .Ldmab2
	s_add_i32 s42, s7, s90
	v_lshl_add_u64 v[252:253], s[40:41], 0, v[214:215]
	s_add_i32 m0, s42, 0x400
	s_nop 0
	global_load_lds_dwordx4 v[252:253], off
.Ldmab2:
	ds_read_b64_tr_b16 v[156:157], v0 offset:0x1400
	ds_read_b64_tr_b16 v[158:159], v0 offset:0x1c00
	ds_read_b64_tr_b16 v[168:169], v0 offset:0x1600
	ds_read_b64_tr_b16 v[170:171], v0 offset:0x1e00
	s_waitcnt lgkmcnt(4)
	v_mfma_f32_32x32x16_bf16 v[112:127], v[10:13], v[160:163], v[112:127]
	v_mfma_f32_32x32x16_bf16 v[96:111], v[10:13], v[164:167], v[96:111]
	v_mfma_f32_32x32x16_bf16 v[128:143], v[152:155], v[160:163], v[128:143]
	v_mfma_f32_32x32x16_bf16 v[80:95], v[152:155], v[164:167], v[80:95]
	s_cmp_gt_u32 s86, 61
	s_cbranch_scc1 .Ldmab3
	s_add_i32 s42, s3, s90
	v_lshl_add_u64 v[252:253], s[40:41], 0, v[216:217]
	v_lshl_add_u64 v[252:253], v[252:253], 0, s[24:25]
	s_mov_b32 m0, s42
	s_nop 0
	global_load_lds_dwordx4 v[252:253], off
.Ldmab3:
	ds_read_b64_tr_b16 v[160:161], v0 offset:0x2000
	ds_read_b64_tr_b16 v[162:163], v0 offset:0x2800
	ds_read_b64_tr_b16 v[164:165], v0 offset:0x2200
	ds_read_b64_tr_b16 v[166:167], v0 offset:0x2a00
	s_waitcnt lgkmcnt(4)
	v_mfma_f32_32x32x16_bf16 v[64:79], v[10:13], v[156:159], v[64:79]
	v_mfma_f32_32x32x16_bf16 v[48:63], v[10:13], v[168:171], v[48:63]
	v_mfma_f32_32x32x16_bf16 v[32:47], v[152:155], v[156:159], v[32:47]
	v_mfma_f32_32x32x16_bf16 v[16:31], v[152:155], v[168:171], v[16:31]
	s_cmp_gt_u32 s86, 61
	s_cbranch_scc1 .Ldmab4
	s_add_i32 s42, s3, s90
	v_lshl_add_u64 v[252:253], s[40:41], 0, v[216:217]
	v_lshl_add_u64 v[252:253], v[252:253], 0, s[26:27]
	s_add_i32 m0, s42, 0x400
	s_nop 0
	global_load_lds_dwordx4 v[252:253], off
.Ldmab4:
	ds_read_b64_tr_b16 v[10:11], v0 offset:0x2400
	ds_read_b64_tr_b16 v[12:13], v0 offset:0x2c00
	ds_read_b64_tr_b16 v[152:153], v0 offset:0x2600
	ds_read_b64_tr_b16 v[154:155], v0 offset:0x2e00
	s_waitcnt lgkmcnt(4)
	v_mfma_f32_32x32x16_bf16 v[112:127], v[6:9], v[160:163], v[112:127]
	v_mfma_f32_32x32x16_bf16 v[96:111], v[6:9], v[164:167], v[96:111]
	v_mfma_f32_32x32x16_bf16 v[128:143], v[148:151], v[160:163], v[128:143]
	v_mfma_f32_32x32x16_bf16 v[80:95], v[148:151], v[164:167], v[80:95]
	ds_read_b64_tr_b16 v[156:157], v0 offset:0x3000
	ds_read_b64_tr_b16 v[158:159], v0 offset:0x3800
	ds_read_b64_tr_b16 v[160:161], v0 offset:0x3200
	ds_read_b64_tr_b16 v[162:163], v0 offset:0x3a00
	s_waitcnt lgkmcnt(4)
	v_mfma_f32_32x32x16_bf16 v[64:79], v[6:9], v[10:13], v[64:79]
	v_mfma_f32_32x32x16_bf16 v[48:63], v[6:9], v[152:155], v[48:63]
	v_mfma_f32_32x32x16_bf16 v[32:47], v[148:151], v[10:13], v[32:47]
	v_mfma_f32_32x32x16_bf16 v[16:31], v[148:151], v[152:155], v[16:31]
	ds_read_b64_tr_b16 v[6:7], v0 offset:0x3400
	ds_read_b64_tr_b16 v[8:9], v0 offset:0x3c00
	ds_read_b64_tr_b16 v[10:11], v0 offset:0x3600
	ds_read_b64_tr_b16 v[12:13], v0 offset:0x3e00
	s_waitcnt lgkmcnt(4)
	v_mfma_f32_32x32x16_bf16 v[112:127], v[2:5], v[156:159], v[112:127]
	v_mfma_f32_32x32x16_bf16 v[96:111], v[2:5], v[160:163], v[96:111]
	v_mfma_f32_32x32x16_bf16 v[128:143], v[144:147], v[156:159], v[128:143]
	v_mfma_f32_32x32x16_bf16 v[80:95], v[144:147], v[160:163], v[80:95]
	s_waitcnt lgkmcnt(0)
	v_mfma_f32_32x32x16_bf16 v[64:79], v[2:5], v[6:9], v[64:79]
	v_mfma_f32_32x32x16_bf16 v[48:63], v[2:5], v[10:13], v[48:63]
	v_mfma_f32_32x32x16_bf16 v[32:47], v[144:147], v[6:9], v[32:47]
	v_mfma_f32_32x32x16_bf16 v[16:31], v[144:147], v[10:13], v[16:31]

.LBB0_205:
	v_add_u32_e32 v219, v212, v232
	v_add_u32_e32 v212, v212, v233
	s_waitcnt lgkmcnt(0)
	v_mfma_f32_32x32x16_bf16 v[144:159], v[248:251], v[192:195], v[144:159]
	ds_read_b128 v[248:251], v219
	v_mfma_f32_32x32x16_bf16 v[160:175], v[236:239], v[192:195], v[160:175]
	ds_read_b128 v[236:239], v219 offset:8192
	v_mfma_f32_32x32x16_bf16 v[144:159], v[240:243], v[196:199], v[144:159]
	ds_read_b128 v[240:243], v212
	v_mfma_f32_32x32x16_bf16 v[160:175], v[244:247], v[196:199], v[160:175]
	ds_read_b128 v[244:247], v212 offset:8192
	s_waitcnt lgkmcnt(3)
	v_mfma_f32_32x32x16_bf16 v[144:159], v[248:251], v[200:203], v[144:159]
	s_waitcnt lgkmcnt(2)
	v_mfma_f32_32x32x16_bf16 v[160:175], v[236:239], v[200:203], v[160:175]
	v_add_f32_e32 v212, v213, v218
	v_add_f32_e32 v235, v235, v212
	s_waitcnt lgkmcnt(1)
	v_mfma_f32_32x32x16_bf16 v[144:159], v[240:243], v[204:207], v[144:159]
	s_waitcnt lgkmcnt(0)
	v_mfma_f32_32x32x16_bf16 v[160:175], v[244:247], v[204:207], v[160:175]
	s_nop 10
	v_exp_f32_e32 v212, v144
	v_exp_f32_e32 v218, v145
	v_exp_f32_e32 v242, v148
	v_exp_f32_e32 v244, v149
	v_exp_f32_e32 v213, v152
	v_exp_f32_e32 v219, v153
	v_exp_f32_e32 v243, v156
	v_exp_f32_e32 v245, v157
	v_exp_f32_e32 v236, v146
	v_exp_f32_e32 v150, v150
	v_exp_f32_e32 v248, v151
	v_exp_f32_e32 v237, v154
	v_exp_f32_e32 v151, v158
	v_exp_f32_e32 v238, v147
	v_exp_f32_e32 v239, v155
	v_exp_f32_e32 v249, v159
	v_exp_f32_e32 v160, v160
	v_exp_f32_e32 v220, v161
	v_exp_f32_e32 v164, v164
	v_exp_f32_e32 v246, v165
	v_exp_f32_e32 v161, v168
	v_exp_f32_e32 v165, v172
	v_exp_f32_e32 v221, v169
	v_exp_f32_e32 v247, v173
	v_pk_add_f32 v[144:145], v[212:213], v[218:219]
	v_pk_add_f32 v[146:147], v[242:243], v[244:245]
	v_exp_f32_e32 v162, v162
	v_exp_f32_e32 v240, v163
	v_exp_f32_e32 v166, v166
	v_exp_f32_e32 v250, v167
	v_exp_f32_e32 v163, v170
	v_exp_f32_e32 v167, v174
	v_pk_add_f32 v[144:145], v[236:237], v[144:145]
	v_pk_add_f32 v[146:147], v[150:151], v[146:147]
	v_exp_f32_e32 v241, v171
	v_exp_f32_e32 v251, v175
	v_pk_add_f32 v[144:145], v[238:239], v[144:145]
	v_pk_add_f32 v[146:147], v[248:249], v[146:147]
	v_pk_add_f32 v[144:145], v[160:161], v[144:145]
	v_pk_add_f32 v[146:147], v[164:165], v[146:147]
	v_pk_add_f32 v[144:145], v[220:221], v[144:145]
	v_pk_add_f32 v[146:147], v[246:247], v[146:147]
	v_pk_add_f32 v[144:145], v[162:163], v[144:145]
	v_pk_add_f32 v[146:147], v[166:167], v[146:147]
	v_pk_add_f32 v[144:145], v[240:241], v[144:145]
	v_pk_add_f32 v[146:147], v[250:251], v[146:147]
	v_cvt_pk_bf16_f32 v148, v213, v219
	v_pk_add_f32 v[144:145], v[144:145], v[146:147]
	v_cvt_pk_bf16_f32 v146, v242, v244
	v_pk_add_f32 v[144:145], v[144:145], v[144:145] op_sel:[0,1] op_sel_hi:[1,0]
	v_cvt_pk_bf16_f32 v147, v150, v248
	v_mov_b32_e32 v145, v144
	s_nop 1
	v_permlane32_swap_b32_e32 v144, v145
	v_add_f32_e32 v144, v144, v145
	v_add_f32_e32 v234, v234, v144
	v_cvt_pk_bf16_f32 v144, v212, v218
	v_cvt_pk_bf16_f32 v145, v236, v238
	v_cvt_pk_bf16_f32 v149, v237, v239
	v_cvt_pk_bf16_f32 v150, v243, v245
	v_cvt_pk_bf16_f32 v151, v151, v249
	v_cvt_pk_bf16_f32 v152, v160, v220
	v_cvt_pk_bf16_f32 v153, v162, v240
	v_cvt_pk_bf16_f32 v154, v164, v246
	v_cvt_pk_bf16_f32 v155, v166, v250
	v_cvt_pk_bf16_f32 v156, v161, v221
	v_cvt_pk_bf16_f32 v157, v163, v241
	v_cvt_pk_bf16_f32 v158, v165, v247
	v_cvt_pk_bf16_f32 v159, v167, v251
	v_permlane32_swap_b32_e32 v144, v146
	v_permlane32_swap_b32_e32 v145, v147
	v_permlane32_swap_b32_e32 v148, v150
	v_permlane32_swap_b32_e32 v149, v151
	v_permlane32_swap_b32_e32 v152, v154
	v_permlane32_swap_b32_e32 v153, v155
	v_permlane32_swap_b32_e32 v156, v158
	v_permlane32_swap_b32_e32 v157, v159
	s_waitcnt lgkmcnt(0)
	v_add_u32_e32 v212, s56, v224
	ds_read_b64_tr_b16 v[160:161], v212 offset:0
	ds_read_b64_tr_b16 v[162:163], v212 offset:0x800
	ds_read_b64_tr_b16 v[164:165], v212 offset:0x200
	ds_read_b64_tr_b16 v[166:167], v212 offset:0xa00
	ds_read_b64_tr_b16 v[168:169], v212 offset:0x400
	ds_read_b64_tr_b16 v[170:171], v212 offset:0xc00
	ds_read_b64_tr_b16 v[172:173], v212 offset:0x600
	ds_read_b64_tr_b16 v[174:175], v212 offset:0xe00
	s_waitcnt lgkmcnt(4)
	s_nop 0
	v_mfma_f32_32x32x16_bf16 v[112:127], v[208:211], v[160:163], v[112:127]
	v_mfma_f32_32x32x16_bf16 v[96:111], v[208:211], v[164:167], v[96:111]
	v_mfma_f32_32x32x16_bf16 v[128:143], v[144:147], v[160:163], v[128:143]
	v_mfma_f32_32x32x16_bf16 v[80:95], v[144:147], v[164:167], v[80:95]
	s_cmp_gt_u32 s71, 61
	s_cbranch_scc1 .Ldmaa1
	s_add_i32 s42, s7, s90
	v_lshl_add_u64 v[252:253], s[40:41], 0, v[216:217]
	s_mov_b32 m0, s42
	s_nop 0
	global_load_lds_dwordx4 v[252:253], off
.Ldmaa1:
	ds_read_b64_tr_b16 v[160:161], v212 offset:0x1000
	ds_read_b64_tr_b16 v[162:163], v212 offset:0x1800
	ds_read_b64_tr_b16 v[164:165], v212 offset:0x1200
	ds_read_b64_tr_b16 v[166:167], v212 offset:0x1a00
	s_waitcnt lgkmcnt(4)
	v_mfma_f32_32x32x16_bf16 v[64:79], v[208:211], v[168:171], v[64:79]
	v_mfma_f32_32x32x16_bf16 v[48:63], v[208:211], v[172:175], v[48:63]
	v_mfma_f32_32x32x16_bf16 v[32:47], v[144:147], v[168:171], v[32:47]
	v_mfma_f32_32x32x16_bf16 v[16:31], v[144:147], v[172:175], v[16:31]
	s_cmp_gt_u32 s71, 61
	s_cbranch_scc1 .Ldmaa2
	s_add_i32 s42, s7, s90
	v_lshl_add_u64 v[252:253], s[40:41], 0, v[214:215]
	s_add_i32 m0, s42, 0x400
	s_nop 0
	global_load_lds_dwordx4 v[252:253], off
.Ldmaa2:
	ds_read_b64_tr_b16 v[144:145], v212 offset:0x1400
	ds_read_b64_tr_b16 v[146:147], v212 offset:0x1c00
	ds_read_b64_tr_b16 v[168:169], v212 offset:0x1600
	ds_read_b64_tr_b16 v[170:171], v212 offset:0x1e00
	s_waitcnt lgkmcnt(4)
	v_mfma_f32_32x32x16_bf16 v[112:127], v[10:13], v[160:163], v[112:127]
	v_mfma_f32_32x32x16_bf16 v[96:111], v[10:13], v[164:167], v[96:111]
	v_mfma_f32_32x32x16_bf16 v[128:143], v[148:151], v[160:163], v[128:143]
	v_mfma_f32_32x32x16_bf16 v[80:95], v[148:151], v[164:167], v[80:95]
	s_cmp_gt_u32 s71, 61
	s_cbranch_scc1 .Ldmaa3
	s_add_i32 s42, s3, s90
	v_lshl_add_u64 v[252:253], s[40:41], 0, v[14:15]
	v_lshl_add_u64 v[252:253], v[252:253], 0, s[24:25]
	s_mov_b32 m0, s42
	s_nop 0
	global_load_lds_dwordx4 v[252:253], off
.Ldmaa3:
	ds_read_b64_tr_b16 v[160:161], v212 offset:0x2000
	ds_read_b64_tr_b16 v[162:163], v212 offset:0x2800
	ds_read_b64_tr_b16 v[164:165], v212 offset:0x2200
	ds_read_b64_tr_b16 v[166:167], v212 offset:0x2a00
	s_waitcnt lgkmcnt(4)
	v_mfma_f32_32x32x16_bf16 v[64:79], v[10:13], v[144:147], v[64:79]
	v_mfma_f32_32x32x16_bf16 v[48:63], v[10:13], v[168:171], v[48:63]
	v_mfma_f32_32x32x16_bf16 v[32:47], v[148:151], v[144:147], v[32:47]
	v_mfma_f32_32x32x16_bf16 v[16:31], v[148:151], v[168:171], v[16:31]
	s_cmp_gt_u32 s71, 61
	s_cbranch_scc1 .Ldmaa4
	s_add_i32 s42, s3, s90
	v_lshl_add_u64 v[252:253], s[40:41], 0, v[14:15]
	v_lshl_add_u64 v[252:253], v[252:253], 0, s[26:27]
	s_add_i32 m0, s42, 0x400
	s_nop 0
	global_load_lds_dwordx4 v[252:253], off
.Ldmaa4:
	ds_read_b64_tr_b16 v[10:11], v212 offset:0x2400
	ds_read_b64_tr_b16 v[12:13], v212 offset:0x2c00
	ds_read_b64_tr_b16 v[144:145], v212 offset:0x2600
	ds_read_b64_tr_b16 v[146:147], v212 offset:0x2e00
	s_waitcnt lgkmcnt(4)
	v_mfma_f32_32x32x16_bf16 v[112:127], v[6:9], v[160:163], v[112:127]
	v_mfma_f32_32x32x16_bf16 v[96:111], v[6:9], v[164:167], v[96:111]
	v_mfma_f32_32x32x16_bf16 v[128:143], v[152:155], v[160:163], v[128:143]
	v_mfma_f32_32x32x16_bf16 v[80:95], v[152:155], v[164:167], v[80:95]
	ds_read_b64_tr_b16 v[148:149], v212 offset:0x3000
	ds_read_b64_tr_b16 v[150:151], v212 offset:0x3800
	ds_read_b64_tr_b16 v[160:161], v212 offset:0x3200
	ds_read_b64_tr_b16 v[162:163], v212 offset:0x3a00
	s_waitcnt lgkmcnt(4)
	v_mfma_f32_32x32x16_bf16 v[64:79], v[6:9], v[10:13], v[64:79]
	v_mfma_f32_32x32x16_bf16 v[48:63], v[6:9], v[144:147], v[48:63]
	v_mfma_f32_32x32x16_bf16 v[32:47], v[152:155], v[10:13], v[32:47]
	v_mfma_f32_32x32x16_bf16 v[16:31], v[152:155], v[144:147], v[16:31]
	ds_read_b64_tr_b16 v[6:7], v212 offset:0x3400
	ds_read_b64_tr_b16 v[8:9], v212 offset:0x3c00
	ds_read_b64_tr_b16 v[10:11], v212 offset:0x3600
	ds_read_b64_tr_b16 v[12:13], v212 offset:0x3e00
	s_waitcnt lgkmcnt(4)
	v_mfma_f32_32x32x16_bf16 v[112:127], v[2:5], v[148:151], v[112:127]
	v_mfma_f32_32x32x16_bf16 v[96:111], v[2:5], v[160:163], v[96:111]
	v_mfma_f32_32x32x16_bf16 v[128:143], v[156:159], v[148:151], v[128:143]
	v_mfma_f32_32x32x16_bf16 v[80:95], v[156:159], v[160:163], v[80:95]
	s_waitcnt lgkmcnt(0)
	v_mfma_f32_32x32x16_bf16 v[64:79], v[2:5], v[6:9], v[64:79]
	v_mfma_f32_32x32x16_bf16 v[48:63], v[2:5], v[10:13], v[48:63]
	v_mfma_f32_32x32x16_bf16 v[32:47], v[156:159], v[6:9], v[32:47]
	v_mfma_f32_32x32x16_bf16 v[16:31], v[156:159], v[10:13], v[16:31]
	s_add_i32 s42, s56, 0x4000
	s_cmpk_lg_u32 s56, 0xc000
	s_cselect_b32 s56, s42, 0
	s_add_i32 s42, s90, 0x4000
	s_cmpk_lg_u32 s90, 0xc000
	s_cselect_b32 s90, s42, 0
	s_add_u32 s40, s40, 0x60000
	s_addc_u32 s41, s41, 0
	s_addk_i32 s73, 0x100
	s_add_i32 s72, s72, 64
	s_add_i32 s71, s71, 1
	s_cmpk_eq_i32 s73, 0x4000
	s_cbranch_scc1 .LBB0_220

.LBB0_208:
.LBB0_210:
	s_add_i32 s44, s72, 0xfffffdb2
	s_cmp_gt_u32 s44, 0xfffffb44
	s_cselect_b64 s[42:43], -1, 0
	s_cmp_lt_u32 s44, 0xfffffb45
	s_cselect_b64 vcc, -1, 0
	s_cmp_gt_i32 s72, -1
	s_cselect_b64 s[44:45], -1, 0
	s_xor_b64 s[44:45], s[0:1], s[44:45]
	v_add_u32_e32 v219, s73, v0
	s_and_b64 s[44:45], vcc, s[44:45]
	v_add_u32_e32 v220, 0x21700, v219
	s_and_b64 vcc, exec, vcc
	s_cbranch_vccnz .LBB0_214
	v_add_u32_e32 v2, 0x21780, v219
	v_add_u32_e32 v3, 0x21708, v219
	v_add_u32_e32 v4, 0x21788, v219
	ds_read2_b32 v[160:161], v220 offset1:1
	ds_read2_b32 v[144:145], v2 offset1:1
	ds_read2_b32 v[162:163], v3 offset1:1
	ds_read2_b32 v[146:147], v4 offset1:1
	v_add_u32_e32 v2, 0x21720, v219
	v_add_u32_e32 v3, 0x217a0, v219
	v_add_u32_e32 v4, 0x21728, v219
	v_add_u32_e32 v5, 0x217a8, v219
	ds_read2_b32 v[164:165], v2 offset1:1
	ds_read2_b32 v[148:149], v3 offset1:1
	ds_read2_b32 v[166:167], v4 offset1:1
	ds_read2_b32 v[150:151], v5 offset1:1
	v_add_u32_e32 v2, 0x21740, v219
	v_add_u32_e32 v3, 0x217c0, v219
	v_add_u32_e32 v4, 0x21748, v219
	v_add_u32_e32 v5, 0x217c8, v219
	ds_read2_b32 v[168:169], v2 offset1:1
	ds_read2_b32 v[152:153], v3 offset1:1
	ds_read2_b32 v[170:171], v4 offset1:1
	ds_read2_b32 v[154:155], v5 offset1:1
	v_add_u32_e32 v2, 0x21760, v219
	v_add_u32_e32 v3, 0x217e0, v219
	v_add_u32_e32 v4, 0x21768, v219
	v_add_u32_e32 v5, 0x217e8, v219
	ds_read2_b32 v[172:173], v2 offset1:1
	ds_read2_b32 v[156:157], v3 offset1:1
	ds_read2_b32 v[174:175], v4 offset1:1
	ds_read2_b32 v[158:159], v5 offset1:1
	s_branch .LBB0_215

.LBB0_213:
	s_waitcnt vmcnt(0) lgkmcnt(0)
	s_barrier
	s_branch .LBB0_210
